# speedup vs baseline: 1.0053x; 1.0053x over previous
.LBB3_25:
	s_waitcnt vmcnt(7) lgkmcnt(3)
	v_mfma_f32_32x32x16_f16 v[18:33], v[34:37], v[114:117], v[18:33]
	s_waitcnt lgkmcnt(2)
	v_mfma_f32_32x32x16_f16 v[2:17], v[34:37], v[110:113], v[2:17]
	global_load_dwordx4 v[34:37], v[98:99], off
	ds_read_b128 v[110:113], v203
	ds_read_b128 v[114:117], v203 offset:33280
	s_waitcnt vmcnt(7) lgkmcnt(3)
	v_mfma_f32_32x32x16_f16 v[18:33], v[38:41], v[106:109], v[18:33]
	s_waitcnt lgkmcnt(2)
	v_mfma_f32_32x32x16_f16 v[2:17], v[38:41], v[102:105], v[2:17]
	global_load_dwordx4 v[38:41], v[98:99], off offset:1024
	ds_read_b128 v[100:103], v203 offset:32
	ds_read_b128 v[104:107], v203 offset:33312
	s_waitcnt vmcnt(7) lgkmcnt(3)
	v_mfma_f32_32x32x16_f16 v[18:33], v[42:45], v[110:113], v[18:33]
	s_waitcnt lgkmcnt(2)
	v_mfma_f32_32x32x16_f16 v[2:17], v[42:45], v[114:117], v[2:17]
	global_load_dwordx4 v[42:45], v[98:99], off offset:2048
	ds_read_b128 v[108:111], v203 offset:64
	ds_read_b128 v[112:115], v203 offset:33344
	s_waitcnt vmcnt(7) lgkmcnt(3)
	v_mfma_f32_32x32x16_f16 v[18:33], v[46:49], v[100:103], v[18:33]
	s_waitcnt lgkmcnt(2)
	v_mfma_f32_32x32x16_f16 v[2:17], v[46:49], v[104:107], v[2:17]
	global_load_dwordx4 v[46:49], v[98:99], off offset:3072
	ds_read_b128 v[100:103], v203 offset:96
	ds_read_b128 v[104:107], v203 offset:33376
	s_waitcnt vmcnt(7) lgkmcnt(3)
	v_mfma_f32_32x32x16_f16 v[18:33], v[54:57], v[108:111], v[18:33]
	v_add_co_u32_e32 v108, vcc, s9, v98
	v_lshl_add_u64 v[118:119], v[98:99], 0, s[6:7]
	s_nop 0
	v_addc_co_u32_e32 v109, vcc, 0, v99, vcc
	s_waitcnt lgkmcnt(2)
	v_mfma_f32_32x32x16_f16 v[2:17], v[54:57], v[112:115], v[2:17]
	global_load_dwordx4 v[54:57], v[108:109], off
	ds_read_b128 v[108:111], v203 offset:128
	ds_read_b128 v[112:115], v203 offset:33408
	s_waitcnt vmcnt(7) lgkmcnt(3)
	v_mfma_f32_32x32x16_f16 v[18:33], v[50:53], v[100:103], v[18:33]
	s_waitcnt lgkmcnt(2)
	v_mfma_f32_32x32x16_f16 v[2:17], v[50:53], v[104:107], v[2:17]
	global_load_dwordx4 v[50:53], v[118:119], off offset:1024
	ds_read_b128 v[100:103], v203 offset:160
	ds_read_b128 v[104:107], v203 offset:33440
	s_waitcnt vmcnt(7) lgkmcnt(3)
	v_mfma_f32_32x32x16_f16 v[18:33], v[58:61], v[108:111], v[18:33]
	s_waitcnt lgkmcnt(2)
	v_mfma_f32_32x32x16_f16 v[2:17], v[58:61], v[112:115], v[2:17]
	global_load_dwordx4 v[58:61], v[118:119], off offset:2048
	ds_read_b128 v[114:117], v203 offset:192
	ds_read_b128 v[110:113], v203 offset:33472
	s_waitcnt vmcnt(7) lgkmcnt(3)
	v_mfma_f32_32x32x16_f16 v[18:33], v[62:65], v[100:103], v[18:33]
	s_waitcnt lgkmcnt(2)
	v_mfma_f32_32x32x16_f16 v[2:17], v[62:65], v[104:107], v[2:17]
	global_load_dwordx4 v[62:65], v[118:119], off offset:3072
	ds_read_b128 v[106:109], v203 offset:224
	ds_read_b128 v[102:105], v203 offset:33504
	s_add_i32 s3, s3, 8
	s_cmp_lt_u32 s3, 16
	v_add_u32_e32 v203, 0x100, v203
	v_lshl_add_u64 v[98:99], v[98:99], 0, s[0:1]
	s_cbranch_scc1 .LBB3_25
	v_add_u32_e32 v118, v189, v150
	s_waitcnt vmcnt(7) lgkmcnt(3)
	v_mfma_f32_32x32x16_f16 v[18:33], v[34:37], v[114:117], v[18:33]
	ds_read_b128 v[98:101], v118 offset:832
	ds_read_b128 v[114:117], v118 offset:34112
	s_waitcnt lgkmcnt(4)
	v_mfma_f32_32x32x16_f16 v[2:17], v[34:37], v[110:113], v[2:17]
	s_waitcnt vmcnt(6) lgkmcnt(3)
	v_mfma_f32_32x32x16_f16 v[18:33], v[38:41], v[106:109], v[18:33]
	ds_read_b128 v[34:37], v118 offset:864
	ds_read_b128 v[106:109], v118 offset:34144
	s_waitcnt lgkmcnt(4)
	v_mfma_f32_32x32x16_f16 v[2:17], v[38:41], v[102:105], v[2:17]
	s_waitcnt vmcnt(5) lgkmcnt(3)
	v_mfma_f32_32x32x16_f16 v[18:33], v[42:45], v[98:101], v[18:33]
	ds_read_b128 v[38:41], v118 offset:896
	ds_read_b128 v[98:101], v118 offset:34176
	s_waitcnt lgkmcnt(4)
	v_mfma_f32_32x32x16_f16 v[2:17], v[42:45], v[114:117], v[2:17]
	s_waitcnt vmcnt(4) lgkmcnt(3)
	v_mfma_f32_32x32x16_f16 v[18:33], v[46:49], v[34:37], v[18:33]
	ds_read_b128 v[34:37], v118 offset:928
	ds_read_b128 v[42:45], v118 offset:34208
	s_waitcnt lgkmcnt(4)
	v_mfma_f32_32x32x16_f16 v[2:17], v[46:49], v[106:109], v[2:17]
	s_waitcnt vmcnt(3) lgkmcnt(3)
	v_mfma_f32_32x32x16_f16 v[18:33], v[54:57], v[38:41], v[18:33]
	ds_read_b128 v[38:41], v118 offset:960
	ds_read_b128 v[46:49], v118 offset:34240
	s_waitcnt lgkmcnt(4)
	v_mfma_f32_32x32x16_f16 v[2:17], v[54:57], v[98:101], v[2:17]
	s_waitcnt vmcnt(2) lgkmcnt(3)
	v_mfma_f32_32x32x16_f16 v[18:33], v[50:53], v[34:37], v[18:33]
	ds_read_b128 v[34:37], v118 offset:992
	ds_read_b128 v[54:57], v118 offset:34272
	s_waitcnt lgkmcnt(4)
	v_mfma_f32_32x32x16_f16 v[2:17], v[50:53], v[42:45], v[2:17]
	s_waitcnt vmcnt(1) lgkmcnt(3)
	v_mfma_f32_32x32x16_f16 v[18:33], v[58:61], v[38:41], v[18:33]
	s_waitcnt lgkmcnt(2)
	v_mfma_f32_32x32x16_f16 v[2:17], v[58:61], v[46:49], v[2:17]
	s_waitcnt vmcnt(0) lgkmcnt(1)
	v_mfma_f32_32x32x16_f16 v[18:33], v[62:65], v[34:37], v[18:33]
	s_waitcnt lgkmcnt(0)
	v_mfma_f32_32x32x16_f16 v[2:17], v[62:65], v[54:57], v[2:17]
	v_lshlrev_b32_e32 v38, 2, v191
	s_add_i32 s0, 0, 0x13000
	v_add_u32_e32 v52, s0, v38
	ds_read_b128 v[34:37], v52
	v_lshl_add_u32 v52, v194, 2, s0
	ds_read_b128 v[40:43], v52
	v_lshl_add_u32 v52, v200, 2, s0
	ds_read_b128 v[44:47], v52
	v_lshl_add_u32 v52, v201, 2, s0
	ds_read_b128 v[48:51], v52
	v_add3_u32 v38, 0, v38, v187
	s_and_b32 s5, s5, 0xffff
	s_mov_b32 s7, 0x20000
	s_mov_b32 s6, 0x1000000
	s_waitcnt lgkmcnt(0)
	s_barrier
	v_pk_add_f32 v[18:19], v[34:35], v[18:19]
	v_pk_add_f32 v[20:21], v[36:37], v[20:21]
	v_pk_add_f32 v[2:3], v[34:35], v[2:3]
	v_pk_add_f32 v[4:5], v[36:37], v[4:5]
	ds_write_b128 v38, v[18:21]
	ds_write_b128 v38, v[2:5] offset:33280
	v_pk_add_f32 v[22:23], v[40:41], v[22:23]
	v_pk_add_f32 v[24:25], v[42:43], v[24:25]
	v_pk_add_f32 v[6:7], v[40:41], v[6:7]
	v_pk_add_f32 v[8:9], v[42:43], v[8:9]
	ds_write_b128 v38, v[22:25] offset:32
	ds_write_b128 v38, v[6:9] offset:33312
	v_pk_add_f32 v[26:27], v[44:45], v[26:27]
	v_pk_add_f32 v[28:29], v[46:47], v[28:29]
	v_pk_add_f32 v[10:11], v[44:45], v[10:11]
	v_pk_add_f32 v[12:13], v[46:47], v[12:13]
	ds_write_b128 v38, v[26:29] offset:64
	ds_write_b128 v38, v[10:13] offset:33344
	v_pk_add_f32 v[30:31], v[48:49], v[30:31]
	v_pk_add_f32 v[32:33], v[50:51], v[32:33]
	v_pk_add_f32 v[14:15], v[48:49], v[14:15]
	v_pk_add_f32 v[16:17], v[50:51], v[16:17]
	ds_write_b128 v38, v[30:33] offset:96
	ds_write_b128 v38, v[14:17] offset:33376
	v_lshl_add_u32 v10, v188, 2, 0
	s_lshl_b32 s0, s2, 16
	v_lshl_or_b32 v0, v0, 4, s0
	v_add_u32_e32 v2, v10, v199
	s_waitcnt lgkmcnt(0)
	s_barrier
	ds_read_b128 v[2:5], v2
	v_add_u32_e32 v6, v10, v198
	ds_read_b128 v[6:9], v6
	v_add_u32_e32 v18, v10, v197
	ds_read_b128 v[18:21], v18
	v_add_u32_e32 v22, v10, v195
	ds_read_b128 v[22:25], v22
	v_add_u32_e32 v26, v10, v196
	ds_read_b128 v[26:29], v26
	v_add_u32_e32 v30, v10, v193
	ds_read_b128 v[30:33], v30
	v_add_u32_e32 v34, v10, v192
	ds_read_b128 v[34:37], v34
	v_add_u32_e32 v40, v10, v190
	ds_read_b128 v[40:43], v40
	s_waitcnt lgkmcnt(7)
	v_pk_add_f32 v[2:3], v[2:3], v[90:91]
	v_pk_add_f32 v[4:5], v[4:5], v[92:93]
	buffer_store_dwordx4 v[2:5], v0, s[4:7], 0 offen sc1
	v_lshl_or_b32 v45, v186, 4, s0
	s_waitcnt lgkmcnt(6)
	v_pk_add_f32 v[6:7], v[6:7], v[94:95]
	v_pk_add_f32 v[8:9], v[8:9], v[96:97]
	buffer_store_dwordx4 v[6:9], v45, s[4:7], 0 offen sc1
	v_lshl_or_b32 v46, v182, 4, s0
	s_waitcnt lgkmcnt(5)
	v_pk_add_f32 v[18:19], v[18:19], v[86:87]
	v_pk_add_f32 v[20:21], v[20:21], v[88:89]
	buffer_store_dwordx4 v[18:21], v46, s[4:7], 0 offen sc1
	v_lshl_or_b32 v47, v185, 4, s0
	s_waitcnt lgkmcnt(4)
	v_pk_add_f32 v[22:23], v[22:23], v[82:83]
	v_pk_add_f32 v[24:25], v[24:25], v[84:85]
	buffer_store_dwordx4 v[22:25], v47, s[4:7], 0 offen sc1
	v_lshl_or_b32 v48, v179, 4, s0
	s_waitcnt lgkmcnt(3)
	v_pk_add_f32 v[26:27], v[26:27], v[78:79]
	v_pk_add_f32 v[28:29], v[28:29], v[80:81]
	buffer_store_dwordx4 v[26:29], v48, s[4:7], 0 offen sc1
	v_lshl_or_b32 v49, v184, 4, s0
	s_waitcnt lgkmcnt(2)
	v_pk_add_f32 v[30:31], v[30:31], v[74:75]
	v_pk_add_f32 v[32:33], v[32:33], v[76:77]
	buffer_store_dwordx4 v[30:33], v49, s[4:7], 0 offen sc1
	v_lshl_or_b32 v50, v1, 4, s0
	s_waitcnt lgkmcnt(1)
	v_pk_add_f32 v[34:35], v[34:35], v[70:71]
	v_pk_add_f32 v[36:37], v[36:37], v[72:73]
	buffer_store_dwordx4 v[34:37], v50, s[4:7], 0 offen sc1
	v_lshl_or_b32 v51, v183, 4, s0
	s_waitcnt lgkmcnt(0)
	v_pk_add_f32 v[40:41], v[40:41], v[66:67]
	v_pk_add_f32 v[42:43], v[42:43], v[68:69]
	buffer_store_dwordx4 v[40:43], v51, s[4:7], 0 offen sc1
	s_endpgm
